# hoisted four-waves-per-row scanner without the per-row LDS wait: the prefetched flag is already complete after the wait that precedes the previous row's publish
# speedup vs baseline: 1.0075x; 1.0050x over previous
.Lsc_i3:
	s_mul_i32 s57, s33, 0x9c40
	v_mov_b32_e32 v27, s46
	ds_read_b32 v26, v27
	s_waitcnt lgkmcnt(0)

.Lsc_hasnext:
	v_readfirstlane_b32 s42, v26
	s_cmp_eq_u32 s42, 0
	s_cbranch_scc1 .Lsc_go
